# speedup vs baseline: 1.0055x; 1.0011x over previous
.LBB2_9:
	s_or_b64 exec, exec, s[6:7]
	v_add_u32_e32 v4, 0x1000, v2
	v_mov_b32_e32 v27, -1
	v_cmp_gt_i32_e64 s[4:5], s17, v4
	s_and_saveexec_b64 s[6:7], s[4:5]
	s_cbranch_execz .Lc5_ld
	v_ashrrev_i32_e32 v5, 31, v4
	v_lshl_add_u64 v[4:5], v[4:5], 2, s[14:15]
	global_load_dword v27, v[4:5], off

.LBB2_15:
	s_or_b64 exec, exec, s[12:13]
	v_cmp_lt_i32_e64 s[40:41], -1, v27
	s_and_saveexec_b64 s[42:43], s[40:41]
	v_mov_b32_e32 v28, 2
	v_lshlrev_b32_sdwa v28, v28, v27 dst_sel:DWORD dst_unused:UNUSED_PAD src0_sel:DWORD src1_sel:BYTE_0
	v_mov_b32_e32 v29, 1
	ds_add_u32 v28, v29 offset:4864
	s_or_b64 exec, exec, s[42:43]
	s_add_i32 s3, s16, 0x1400
	s_cmp_lt_i32 s3, s17
	s_cselect_b64 s[18:19], -1, 0
	s_cmp_ge_i32 s3, s17
	s_cbranch_scc1 .LBB2_34
	v_add_u32_e32 v4, 0x1400, v2
	v_ashrrev_i32_e32 v5, 31, v4
	v_lshl_add_u64 v[4:5], v[4:5], 2, s[14:15]
	v_mov_b32_e32 v10, 1
	s_mov_b64 s[20:21], 0x4000
	v_mov_b32_e32 v11, 2
	s_mov_b32 s24, s3
	s_branch .LBB2_18

.LBB2_47:
	s_or_b64 exec, exec, s[6:7]
	s_and_saveexec_b64 s[42:43], s[40:41]
	v_mov_b32_e32 v28, 2
	v_lshlrev_b32_sdwa v28, v28, v27 dst_sel:DWORD dst_unused:UNUSED_PAD src0_sel:DWORD src1_sel:BYTE_0
	v_mov_b32_e32 v29, 1
	ds_add_rtn_u32 v28, v28, v29 offset:4864
	v_lshrrev_b32_e32 v30, 8, v27
	s_waitcnt lgkmcnt(0)
	v_ashrrev_i32_e32 v29, 31, v28
	v_lshl_add_u64 v[28:29], v[28:29], 2, s[20:21]
	global_store_dword v[28:29], v30, off
	s_or_b64 exec, exec, s[42:43]
	s_andn2_b64 vcc, exec, s[18:19]
	s_cbranch_vccz .LBB2_56
	s_branch .LBB2_74

.LBB2_55:
	v_mov_b32_e32 v3, 2
	v_lshlrev_b32_sdwa v3, v3, v1 dst_sel:DWORD dst_unused:UNUSED_PAD src0_sel:DWORD src1_sel:BYTE_0
	v_mov_b32_e32 v4, 1
	ds_add_rtn_u32 v4, v3, v4 offset:4864
	v_lshrrev_b32_e32 v1, 8, v1
	s_waitcnt lgkmcnt(0)
	v_ashrrev_i32_e32 v5, 31, v4
	v_lshl_add_u64 v[4:5], v[4:5], 2, s[20:21]
	global_store_dword v[4:5], v1, off
	s_or_b64 exec, exec, s[6:7]
	s_and_saveexec_b64 s[42:43], s[40:41]
	v_mov_b32_e32 v28, 2
	v_lshlrev_b32_sdwa v28, v28, v27 dst_sel:DWORD dst_unused:UNUSED_PAD src0_sel:DWORD src1_sel:BYTE_0
	v_mov_b32_e32 v29, 1
	ds_add_rtn_u32 v28, v28, v29 offset:4864
	v_lshrrev_b32_e32 v30, 8, v27
	s_waitcnt lgkmcnt(0)
	v_ashrrev_i32_e32 v29, 31, v28
	v_lshl_add_u64 v[28:29], v[28:29], 2, s[20:21]
	global_store_dword v[28:29], v30, off
	s_or_b64 exec, exec, s[42:43]
	s_andn2_b64 vcc, exec, s[18:19]
	s_cbranch_vccnz .LBB2_74
.LBB2_56:
	v_add_u32_e32 v2, 0x1400, v2
	v_ashrrev_i32_e32 v3, 31, v2
	v_lshl_add_u64 v[2:3], v[2:3], 2, s[14:15]
	v_mov_b32_e32 v1, 1
	s_mov_b64 s[4:5], 0x4000
	v_mov_b32_e32 v6, 2
	s_branch .LBB2_58
